# MoE k-loop: A operand in 4 LDS stages, k-tiles t+2 and t+3 requested together at even t so both halves of each 128-B line are fetched once; plus two B staging sets
# speedup vs baseline: 1.0418x; 1.0287x over previous
.LBB0_1174:
	s_setprio 0
	s_add_i32 s5, s5, 1
	s_and_b32 s5, s5, 3
	s_add_i32 s35, s2, 1
	s_barrier
	s_cmp_lg_u32 s2, 2
	s_cselect_b32 s2, s35, 0
	s_add_i32 s34, s34, 1
	v_lshl_add_u64 v[204:205], v[204:205], 0, 64
	v_lshl_add_u64 v[206:207], v[206:207], 0, 64
	v_lshl_add_u64 v[208:209], v[208:209], 0, s[66:67]
.LBB0_1175:
	s_bitcmp0_b32 s34, 0
	s_cselect_b32 s8, s91, 0x10000
	s_cselect_b32 s9, 0x10000, s91
	s_add_i32 s8, s8, 0
	v_add_u32_e32 v1, s8, v214
	v_add_u32_e32 v3, s8, v217
	s_waitcnt lgkmcnt(14)
	ds_read_b64_tr_b16 v[150:151], v1
	ds_read_b64_tr_b16 v[152:153], v1 offset:2048
	ds_read_b64_tr_b16 v[154:155], v3
	ds_read_b64_tr_b16 v[156:157], v3 offset:2048
	v_add_u32_e32 v1, s8, v216
	v_add_u32_e32 v3, s8, v215
	s_waitcnt lgkmcnt(14)
	ds_read_b64_tr_b16 v[158:159], v1
	ds_read_b64_tr_b16 v[160:161], v1 offset:2048
	ds_read_b64_tr_b16 v[162:163], v3
	ds_read_b64_tr_b16 v[164:165], v3 offset:2048
	s_lshl_b32 s35, s5, 14
	s_cmp_eq_u32 s5, 3
	s_cselect_b32 s35, 0x18000, s35
	v_add_u32_e32 v1, s35, v213
	s_waitcnt lgkmcnt(14)
	ds_read_b128 v[194:197], v1
	ds_read_b128 v[190:193], v1 offset:1024
	ds_read_b128 v[186:189], v1 offset:2048
	ds_read_b128 v[182:185], v1 offset:3072
	s_waitcnt lgkmcnt(14)
	ds_read_b128 v[178:181], v1 offset:4096
	ds_read_b128 v[174:177], v1 offset:5120
	ds_read_b128 v[170:173], v1 offset:6144
	ds_read_b128 v[166:169], v1 offset:7168
	s_cmp_eq_u32 s5, 0
	s_cselect_b32 s8, 0x8000, 0
	s_add_i32 s8, s33, s8
	s_mov_b32 s35, m0
	s_mov_b32 m0, s8
	s_nop 0
	global_load_lds_dwordx4 v[206:207], off
	s_mov_b32 m0, s35
	s_addk_i32 s8, 0x2000
	s_mov_b32 s35, m0
	s_mov_b32 m0, s8
	s_nop 0
	global_load_lds_dwordx4 v[204:205], off
	s_mov_b32 m0, s35
	s_cmp_eq_u32 s5, 0
	s_cselect_b32 s8, 0x14000, 0
	s_add_i32 s8, s33, s8
	s_addk_i32 s8, 0x3fc0
	s_mov_b32 s35, m0
	s_mov_b32 m0, s8
	s_nop 0
	global_load_lds_dwordx4 v[206:207], off offset:64
	s_mov_b32 m0, s35
	s_addk_i32 s8, 0x2000
	s_mov_b32 s35, m0
	s_mov_b32 m0, s8
	s_nop 0
	global_load_lds_dwordx4 v[204:205], off offset:64
	s_mov_b32 m0, s35
	v_add_u32_e32 v1, s9, v218
	s_waitcnt vmcnt(8)
	s_nop 0
	v_cvt_pk_bf16_f32 v224, v224, v225
	v_cvt_pk_bf16_f32 v225, v226, v227
	v_cvt_pk_bf16_f32 v226, v228, v229
	v_cvt_pk_bf16_f32 v227, v230, v231
	ds_write_b128 v1, v[224:227]
	v_cvt_pk_bf16_f32 v232, v232, v233
	v_cvt_pk_bf16_f32 v233, v234, v235
	v_cvt_pk_bf16_f32 v234, v236, v237
	v_cvt_pk_bf16_f32 v235, v238, v239
	ds_write_b128 v1, v[232:235] offset:8192
	global_load_dwordx4 v[224:227], v[208:209], off
	global_load_dwordx4 v[228:231], v[208:209], off offset:16
	v_lshl_add_u64 v[4:5], v[208:209], 0, s[62:63]
	global_load_dwordx4 v[232:235], v[4:5], off
	global_load_dwordx4 v[236:239], v[4:5], off offset:16
	s_waitcnt lgkmcnt(0)
	s_barrier
	s_setprio 1
	v_cndmask_b32_e64 v1, 0, 1, s[76:77]
	v_cmp_ne_u32_e64 s[8:9], 1, v1
	s_andn2_b64 vcc, exec, s[76:77]
	s_cbranch_vccnz .Lmoe_end_even
	s_waitcnt lgkmcnt(9)
	v_mfma_f32_16x16x32_bf16 v[146:149], v[150:153], v[194:197], v[146:149]
	v_mfma_f32_16x16x32_bf16 v[142:145], v[154:157], v[194:197], v[142:145]
	v_mfma_f32_16x16x32_bf16 v[138:141], v[158:161], v[194:197], v[138:141]
	v_mfma_f32_16x16x32_bf16 v[134:137], v[162:165], v[194:197], v[134:137]
	s_waitcnt lgkmcnt(8)
	v_mfma_f32_16x16x32_bf16 v[130:133], v[150:153], v[190:193], v[130:133]
	v_mfma_f32_16x16x32_bf16 v[122:125], v[154:157], v[190:193], v[122:125]
	v_mfma_f32_16x16x32_bf16 v[126:129], v[158:161], v[190:193], v[126:129]
	v_mfma_f32_16x16x32_bf16 v[118:121], v[162:165], v[190:193], v[118:121]
	s_waitcnt lgkmcnt(7)
	v_mfma_f32_16x16x32_bf16 v[114:117], v[150:153], v[186:189], v[114:117]
	v_mfma_f32_16x16x32_bf16 v[106:109], v[154:157], v[186:189], v[106:109]
	v_mfma_f32_16x16x32_bf16 v[110:113], v[158:161], v[186:189], v[110:113]
	v_mfma_f32_16x16x32_bf16 v[102:105], v[162:165], v[186:189], v[102:105]
	s_waitcnt lgkmcnt(6)
	v_mfma_f32_16x16x32_bf16 v[98:101], v[150:153], v[182:185], v[98:101]
	v_mfma_f32_16x16x32_bf16 v[90:93], v[154:157], v[182:185], v[90:93]
	v_mfma_f32_16x16x32_bf16 v[94:97], v[158:161], v[182:185], v[94:97]
	v_mfma_f32_16x16x32_bf16 v[86:89], v[162:165], v[182:185], v[86:89]
	s_waitcnt lgkmcnt(5)
	v_mfma_f32_16x16x32_bf16 v[82:85], v[150:153], v[178:181], v[82:85]
	v_mfma_f32_16x16x32_bf16 v[74:77], v[154:157], v[178:181], v[74:77]
	v_mfma_f32_16x16x32_bf16 v[78:81], v[158:161], v[178:181], v[78:81]
	v_mfma_f32_16x16x32_bf16 v[70:73], v[162:165], v[178:181], v[70:73]
	s_waitcnt lgkmcnt(4)
	v_mfma_f32_16x16x32_bf16 v[66:69], v[150:153], v[174:177], v[66:69]
	v_mfma_f32_16x16x32_bf16 v[58:61], v[154:157], v[174:177], v[58:61]
	v_mfma_f32_16x16x32_bf16 v[62:65], v[158:161], v[174:177], v[62:65]
	v_mfma_f32_16x16x32_bf16 v[54:57], v[162:165], v[174:177], v[54:57]
	s_waitcnt lgkmcnt(3)
	v_mfma_f32_16x16x32_bf16 v[50:53], v[150:153], v[170:173], v[50:53]
	v_mfma_f32_16x16x32_bf16 v[42:45], v[154:157], v[170:173], v[42:45]
	v_mfma_f32_16x16x32_bf16 v[46:49], v[158:161], v[170:173], v[46:49]
	v_mfma_f32_16x16x32_bf16 v[38:41], v[162:165], v[170:173], v[38:41]
	s_waitcnt lgkmcnt(2)
	v_mfma_f32_16x16x32_bf16 v[34:37], v[150:153], v[166:169], v[34:37]
	v_mfma_f32_16x16x32_bf16 v[26:29], v[154:157], v[166:169], v[26:29]
	v_mfma_f32_16x16x32_bf16 v[30:33], v[158:161], v[166:169], v[30:33]
	v_mfma_f32_16x16x32_bf16 v[22:25], v[162:165], v[166:169], v[22:25]
.Lmoe_end_even:
	s_setprio 0
	s_add_i32 s5, s5, 1
	s_and_b32 s5, s5, 3
	s_add_i32 s35, s2, 1
	s_barrier
	s_cmp_lg_u32 s2, 2
	s_cselect_b32 s2, s35, 0
	s_add_i32 s34, s34, 1
	v_lshl_add_u64 v[204:205], v[204:205], 0, 64
	v_lshl_add_u64 v[206:207], v[206:207], 0, 64
	v_lshl_add_u64 v[208:209], v[208:209], 0, s[66:67]
	s_cmp_eq_u32 s34, 61
	s_cbranch_scc1 .Lmoe_t61
	s_bitcmp0_b32 s34, 0
	s_cselect_b32 s8, s91, 0x10000
	s_cselect_b32 s9, 0x10000, s91
	s_add_i32 s8, s8, 0
	v_add_u32_e32 v1, s8, v214
	v_add_u32_e32 v3, s8, v217
	s_waitcnt lgkmcnt(14)
	ds_read_b64_tr_b16 v[150:151], v1
	ds_read_b64_tr_b16 v[152:153], v1 offset:2048
	ds_read_b64_tr_b16 v[154:155], v3
	ds_read_b64_tr_b16 v[156:157], v3 offset:2048
	v_add_u32_e32 v1, s8, v216
	v_add_u32_e32 v3, s8, v215
	s_waitcnt lgkmcnt(14)
	ds_read_b64_tr_b16 v[158:159], v1
	ds_read_b64_tr_b16 v[160:161], v1 offset:2048
	ds_read_b64_tr_b16 v[162:163], v3
	ds_read_b64_tr_b16 v[164:165], v3 offset:2048
	s_lshl_b32 s35, s5, 14
	s_cmp_eq_u32 s5, 3
	s_cselect_b32 s35, 0x18000, s35
	v_add_u32_e32 v1, s35, v213
	s_waitcnt lgkmcnt(14)
	ds_read_b128 v[194:197], v1
	ds_read_b128 v[190:193], v1 offset:1024
	ds_read_b128 v[186:189], v1 offset:2048
	ds_read_b128 v[182:185], v1 offset:3072
	s_waitcnt lgkmcnt(14)
	ds_read_b128 v[178:181], v1 offset:4096
	ds_read_b128 v[174:177], v1 offset:5120
	ds_read_b128 v[170:173], v1 offset:6144
	ds_read_b128 v[166:169], v1 offset:7168
	v_add_u32_e32 v1, s9, v218
	s_waitcnt vmcnt(6)
	s_nop 0
	v_cvt_pk_bf16_f32 v18, v18, v19
	v_cvt_pk_bf16_f32 v19, v20, v21
	v_cvt_pk_bf16_f32 v20, v14, v15
	v_cvt_pk_bf16_f32 v21, v16, v17
	ds_write_b128 v1, v[18:21]
	v_cvt_pk_bf16_f32 v4, v10, v11
	v_cvt_pk_bf16_f32 v5, v12, v13
	v_cvt_pk_bf16_f32 v6, v6, v7
	v_cvt_pk_bf16_f32 v7, v8, v9
	ds_write_b128 v1, v[4:7] offset:8192
	global_load_dwordx4 v[18:21], v[208:209], off
	global_load_dwordx4 v[14:17], v[208:209], off offset:16
	v_lshl_add_u64 v[4:5], v[208:209], 0, s[62:63]
	global_load_dwordx4 v[10:13], v[4:5], off
	global_load_dwordx4 v[6:9], v[4:5], off offset:16
	s_waitcnt lgkmcnt(0)
	s_barrier
	s_setprio 1
	v_cndmask_b32_e64 v1, 0, 1, s[76:77]
	v_cmp_ne_u32_e64 s[8:9], 1, v1
	s_andn2_b64 vcc, exec, s[76:77]
	s_cbranch_vccnz .LBB0_1174
	s_waitcnt lgkmcnt(9)
	v_mfma_f32_16x16x32_bf16 v[146:149], v[150:153], v[194:197], v[146:149]
	v_mfma_f32_16x16x32_bf16 v[142:145], v[154:157], v[194:197], v[142:145]
	v_mfma_f32_16x16x32_bf16 v[138:141], v[158:161], v[194:197], v[138:141]
	v_mfma_f32_16x16x32_bf16 v[134:137], v[162:165], v[194:197], v[134:137]
	s_waitcnt lgkmcnt(8)
	v_mfma_f32_16x16x32_bf16 v[130:133], v[150:153], v[190:193], v[130:133]
	v_mfma_f32_16x16x32_bf16 v[122:125], v[154:157], v[190:193], v[122:125]
	v_mfma_f32_16x16x32_bf16 v[126:129], v[158:161], v[190:193], v[126:129]
	v_mfma_f32_16x16x32_bf16 v[118:121], v[162:165], v[190:193], v[118:121]
	s_waitcnt lgkmcnt(7)
	v_mfma_f32_16x16x32_bf16 v[114:117], v[150:153], v[186:189], v[114:117]
	v_mfma_f32_16x16x32_bf16 v[106:109], v[154:157], v[186:189], v[106:109]
	v_mfma_f32_16x16x32_bf16 v[110:113], v[158:161], v[186:189], v[110:113]
	v_mfma_f32_16x16x32_bf16 v[102:105], v[162:165], v[186:189], v[102:105]
	s_waitcnt lgkmcnt(6)
	v_mfma_f32_16x16x32_bf16 v[98:101], v[150:153], v[182:185], v[98:101]
	v_mfma_f32_16x16x32_bf16 v[90:93], v[154:157], v[182:185], v[90:93]
	v_mfma_f32_16x16x32_bf16 v[94:97], v[158:161], v[182:185], v[94:97]
	v_mfma_f32_16x16x32_bf16 v[86:89], v[162:165], v[182:185], v[86:89]
	s_waitcnt lgkmcnt(5)
	v_mfma_f32_16x16x32_bf16 v[82:85], v[150:153], v[178:181], v[82:85]
	v_mfma_f32_16x16x32_bf16 v[74:77], v[154:157], v[178:181], v[74:77]
	v_mfma_f32_16x16x32_bf16 v[78:81], v[158:161], v[178:181], v[78:81]
	v_mfma_f32_16x16x32_bf16 v[70:73], v[162:165], v[178:181], v[70:73]
	s_waitcnt lgkmcnt(4)
	v_mfma_f32_16x16x32_bf16 v[66:69], v[150:153], v[174:177], v[66:69]
	v_mfma_f32_16x16x32_bf16 v[58:61], v[154:157], v[174:177], v[58:61]
	v_mfma_f32_16x16x32_bf16 v[62:65], v[158:161], v[174:177], v[62:65]
	v_mfma_f32_16x16x32_bf16 v[54:57], v[162:165], v[174:177], v[54:57]
	s_waitcnt lgkmcnt(3)
	v_mfma_f32_16x16x32_bf16 v[50:53], v[150:153], v[170:173], v[50:53]
	v_mfma_f32_16x16x32_bf16 v[42:45], v[154:157], v[170:173], v[42:45]
	v_mfma_f32_16x16x32_bf16 v[46:49], v[158:161], v[170:173], v[46:49]
	v_mfma_f32_16x16x32_bf16 v[38:41], v[162:165], v[170:173], v[38:41]
	s_waitcnt lgkmcnt(2)
	v_mfma_f32_16x16x32_bf16 v[34:37], v[150:153], v[166:169], v[34:37]
	v_mfma_f32_16x16x32_bf16 v[26:29], v[154:157], v[166:169], v[26:29]
	v_mfma_f32_16x16x32_bf16 v[30:33], v[158:161], v[166:169], v[30:33]
	v_mfma_f32_16x16x32_bf16 v[22:25], v[162:165], v[166:169], v[22:25]
	s_branch .LBB0_1174
.Lmoe_t61:
	s_bitcmp0_b32 s34, 0
	s_cselect_b32 s8, s91, 0x10000
	s_cselect_b32 s9, 0x10000, s91
	s_add_i32 s8, s8, 0
	v_add_u32_e32 v1, s8, v214
	v_add_u32_e32 v3, s8, v217
	s_waitcnt lgkmcnt(14)
	ds_read_b64_tr_b16 v[150:151], v1
	ds_read_b64_tr_b16 v[152:153], v1 offset:2048
	ds_read_b64_tr_b16 v[154:155], v3
	ds_read_b64_tr_b16 v[156:157], v3 offset:2048
	v_add_u32_e32 v1, s8, v216
	v_add_u32_e32 v3, s8, v215
	s_waitcnt lgkmcnt(14)
	ds_read_b64_tr_b16 v[158:159], v1
	ds_read_b64_tr_b16 v[160:161], v1 offset:2048
	ds_read_b64_tr_b16 v[162:163], v3
	ds_read_b64_tr_b16 v[164:165], v3 offset:2048
	s_lshl_b32 s35, s5, 14
	s_cmp_eq_u32 s5, 3
	s_cselect_b32 s35, 0x18000, s35
	v_add_u32_e32 v1, s35, v213
	s_waitcnt lgkmcnt(14)
	ds_read_b128 v[194:197], v1
	ds_read_b128 v[190:193], v1 offset:1024
	ds_read_b128 v[186:189], v1 offset:2048
	ds_read_b128 v[182:185], v1 offset:3072
	s_waitcnt lgkmcnt(14)
	ds_read_b128 v[178:181], v1 offset:4096
	ds_read_b128 v[174:177], v1 offset:5120
	ds_read_b128 v[170:173], v1 offset:6144
	ds_read_b128 v[166:169], v1 offset:7168
	v_add_u32_e32 v1, s9, v218
	s_waitcnt vmcnt(6)
	s_nop 0
	v_cvt_pk_bf16_f32 v18, v18, v19
	v_cvt_pk_bf16_f32 v19, v20, v21
	v_cvt_pk_bf16_f32 v20, v14, v15
	v_cvt_pk_bf16_f32 v21, v16, v17
	ds_write_b128 v1, v[18:21]
	v_cvt_pk_bf16_f32 v4, v10, v11
	v_cvt_pk_bf16_f32 v5, v12, v13
	v_cvt_pk_bf16_f32 v6, v6, v7
	v_cvt_pk_bf16_f32 v7, v8, v9
	ds_write_b128 v1, v[4:7] offset:8192
	s_waitcnt lgkmcnt(0)
	s_barrier
	s_setprio 1
	v_cndmask_b32_e64 v1, 0, 1, s[76:77]
	v_cmp_ne_u32_e64 s[8:9], 1, v1
	s_andn2_b64 vcc, exec, s[76:77]
	s_cbranch_vccnz .Lmoe_end_t61
	s_waitcnt lgkmcnt(9)
	v_mfma_f32_16x16x32_bf16 v[146:149], v[150:153], v[194:197], v[146:149]
	v_mfma_f32_16x16x32_bf16 v[142:145], v[154:157], v[194:197], v[142:145]
	v_mfma_f32_16x16x32_bf16 v[138:141], v[158:161], v[194:197], v[138:141]
	v_mfma_f32_16x16x32_bf16 v[134:137], v[162:165], v[194:197], v[134:137]
	s_waitcnt lgkmcnt(8)
	v_mfma_f32_16x16x32_bf16 v[130:133], v[150:153], v[190:193], v[130:133]
	v_mfma_f32_16x16x32_bf16 v[122:125], v[154:157], v[190:193], v[122:125]
	v_mfma_f32_16x16x32_bf16 v[126:129], v[158:161], v[190:193], v[126:129]
	v_mfma_f32_16x16x32_bf16 v[118:121], v[162:165], v[190:193], v[118:121]
	s_waitcnt lgkmcnt(7)
	v_mfma_f32_16x16x32_bf16 v[114:117], v[150:153], v[186:189], v[114:117]
	v_mfma_f32_16x16x32_bf16 v[106:109], v[154:157], v[186:189], v[106:109]
	v_mfma_f32_16x16x32_bf16 v[110:113], v[158:161], v[186:189], v[110:113]
	v_mfma_f32_16x16x32_bf16 v[102:105], v[162:165], v[186:189], v[102:105]
	s_waitcnt lgkmcnt(6)
	v_mfma_f32_16x16x32_bf16 v[98:101], v[150:153], v[182:185], v[98:101]
	v_mfma_f32_16x16x32_bf16 v[90:93], v[154:157], v[182:185], v[90:93]
	v_mfma_f32_16x16x32_bf16 v[94:97], v[158:161], v[182:185], v[94:97]
	v_mfma_f32_16x16x32_bf16 v[86:89], v[162:165], v[182:185], v[86:89]
	s_waitcnt lgkmcnt(5)
	v_mfma_f32_16x16x32_bf16 v[82:85], v[150:153], v[178:181], v[82:85]
	v_mfma_f32_16x16x32_bf16 v[74:77], v[154:157], v[178:181], v[74:77]
	v_mfma_f32_16x16x32_bf16 v[78:81], v[158:161], v[178:181], v[78:81]
	v_mfma_f32_16x16x32_bf16 v[70:73], v[162:165], v[178:181], v[70:73]
	s_waitcnt lgkmcnt(4)
	v_mfma_f32_16x16x32_bf16 v[66:69], v[150:153], v[174:177], v[66:69]
	v_mfma_f32_16x16x32_bf16 v[58:61], v[154:157], v[174:177], v[58:61]
	v_mfma_f32_16x16x32_bf16 v[62:65], v[158:161], v[174:177], v[62:65]
	v_mfma_f32_16x16x32_bf16 v[54:57], v[162:165], v[174:177], v[54:57]
	s_waitcnt lgkmcnt(3)
	v_mfma_f32_16x16x32_bf16 v[50:53], v[150:153], v[170:173], v[50:53]
	v_mfma_f32_16x16x32_bf16 v[42:45], v[154:157], v[170:173], v[42:45]
	v_mfma_f32_16x16x32_bf16 v[46:49], v[158:161], v[170:173], v[46:49]
	v_mfma_f32_16x16x32_bf16 v[38:41], v[162:165], v[170:173], v[38:41]
	s_waitcnt lgkmcnt(2)
	v_mfma_f32_16x16x32_bf16 v[34:37], v[150:153], v[166:169], v[34:37]
	v_mfma_f32_16x16x32_bf16 v[26:29], v[154:157], v[166:169], v[26:29]
	v_mfma_f32_16x16x32_bf16 v[30:33], v[158:161], v[166:169], v[30:33]
	v_mfma_f32_16x16x32_bf16 v[22:25], v[162:165], v[166:169], v[22:25]

.LBB0_1177:
	v_add_u32_e32 v1, 0, v214
	v_add_u32_e32 v3, 0, v217
	s_waitcnt lgkmcnt(14)
	ds_read_b64_tr_b16 v[150:151], v1 offset:49152
	ds_read_b64_tr_b16 v[152:153], v1 offset:51200
	ds_read_b64_tr_b16 v[154:155], v3 offset:49152
	ds_read_b64_tr_b16 v[156:157], v3 offset:51200
	v_add_u32_e32 v1, 0, v216
	v_add_u32_e32 v3, 0, v215
	s_waitcnt lgkmcnt(14)
	ds_read_b64_tr_b16 v[158:159], v1 offset:49152
	ds_read_b64_tr_b16 v[160:161], v1 offset:51200
	ds_read_b64_tr_b16 v[162:163], v3 offset:49152
	ds_read_b64_tr_b16 v[164:165], v3 offset:51200
	s_lshl_b32 s35, s5, 14
	s_cmp_eq_u32 s5, 3
	s_cselect_b32 s35, 0x18000, s35
	v_add_u32_e32 v1, s35, v213
	s_waitcnt lgkmcnt(14)
	ds_read_b128 v[194:197], v1
	ds_read_b128 v[190:193], v1 offset:1024
	ds_read_b128 v[186:189], v1 offset:2048
	ds_read_b128 v[182:185], v1 offset:3072
	s_waitcnt lgkmcnt(14)
	ds_read_b128 v[178:181], v1 offset:4096
	ds_read_b128 v[174:177], v1 offset:5120
	ds_read_b128 v[170:173], v1 offset:6144
	ds_read_b128 v[166:169], v1 offset:7168
	v_add_u32_e32 v1, 0x10000, v218
	s_waitcnt vmcnt(0)
	v_mov_b32_e32 v3, 0
	v_cvt_pk_bf16_f32 v204, v224, v225
	v_cvt_pk_bf16_f32 v205, v226, v227
	v_cvt_pk_bf16_f32 v206, v228, v229
	v_cvt_pk_bf16_f32 v207, v230, v231
	ds_write_b128 v1, v[204:207]
	v_add_u32_e32 v1, 0x12000, v218
	v_cvt_pk_bf16_f32 v204, v232, v233
	v_cvt_pk_bf16_f32 v205, v234, v235
	v_cvt_pk_bf16_f32 v206, v236, v237
	v_cvt_pk_bf16_f32 v207, v238, v239
	ds_write_b128 v1, v[204:207]
	s_and_saveexec_b64 s[34:35], s[6:7]
	s_cbranch_execz .LBB0_1179
	s_lshl_b32 s64, s3, 6
	s_lshl_b64 s[76:77], s[64:65], 2
	s_add_u32 s76, s40, s76
	s_addc_u32 s77, s41, s77
	v_mov_b64_e32 v[4:5], s[76:77]
	global_atomic_add v3, v[4:5], v210, off sc0

.LBB0_1181:
	s_setprio 0
	s_add_i32 s2, 0, 0x10000
	s_barrier
	v_add_u32_e32 v1, s2, v214
	v_add_u32_e32 v4, s2, v217
	s_waitcnt lgkmcnt(14)
	ds_read_b64_tr_b16 v[150:151], v1
	ds_read_b64_tr_b16 v[152:153], v1 offset:2048
	ds_read_b64_tr_b16 v[154:155], v4
	ds_read_b64_tr_b16 v[156:157], v4 offset:2048
	v_add_u32_e32 v1, s2, v216
	v_add_u32_e32 v4, s2, v215
	s_waitcnt lgkmcnt(14)
	ds_read_b64_tr_b16 v[158:159], v1
	ds_read_b64_tr_b16 v[160:161], v1 offset:2048
	ds_read_b64_tr_b16 v[162:163], v4
	ds_read_b64_tr_b16 v[164:165], v4 offset:2048
	s_waitcnt lgkmcnt(14)
	v_add_u32_e32 v1, 0x18000, v213
	ds_read_b128 v[194:197], v1
	ds_read_b128 v[190:193], v1 offset:1024
	ds_read_b128 v[186:189], v1 offset:2048
	ds_read_b128 v[182:185], v1 offset:3072
	s_waitcnt lgkmcnt(14)
	ds_read_b128 v[178:181], v1 offset:4096
	ds_read_b128 v[174:177], v1 offset:5120
	ds_read_b128 v[170:173], v1 offset:6144
	ds_read_b128 v[166:169], v1 offset:7168
	s_waitcnt lgkmcnt(0)
	s_barrier
	s_setprio 1
	s_and_b64 vcc, exec, s[8:9]
	s_cbranch_vccnz .LBB0_1183
	s_waitcnt lgkmcnt(7)
	v_mfma_f32_16x16x32_bf16 v[146:149], v[150:153], v[194:197], v[146:149]
	v_mfma_f32_16x16x32_bf16 v[142:145], v[154:157], v[194:197], v[142:145]
	v_mfma_f32_16x16x32_bf16 v[138:141], v[158:161], v[194:197], v[138:141]
	v_mfma_f32_16x16x32_bf16 v[134:137], v[162:165], v[194:197], v[134:137]
	s_waitcnt lgkmcnt(6)
	v_mfma_f32_16x16x32_bf16 v[130:133], v[150:153], v[190:193], v[130:133]
	v_mfma_f32_16x16x32_bf16 v[122:125], v[154:157], v[190:193], v[122:125]
	v_mfma_f32_16x16x32_bf16 v[126:129], v[158:161], v[190:193], v[126:129]
	v_mfma_f32_16x16x32_bf16 v[118:121], v[162:165], v[190:193], v[118:121]
	s_waitcnt lgkmcnt(5)
	v_mfma_f32_16x16x32_bf16 v[114:117], v[150:153], v[186:189], v[114:117]
	v_mfma_f32_16x16x32_bf16 v[106:109], v[154:157], v[186:189], v[106:109]
	v_mfma_f32_16x16x32_bf16 v[110:113], v[158:161], v[186:189], v[110:113]
	v_mfma_f32_16x16x32_bf16 v[102:105], v[162:165], v[186:189], v[102:105]
	s_waitcnt lgkmcnt(4)
	v_mfma_f32_16x16x32_bf16 v[98:101], v[150:153], v[182:185], v[98:101]
	v_mfma_f32_16x16x32_bf16 v[90:93], v[154:157], v[182:185], v[90:93]
	v_mfma_f32_16x16x32_bf16 v[94:97], v[158:161], v[182:185], v[94:97]
	v_mfma_f32_16x16x32_bf16 v[86:89], v[162:165], v[182:185], v[86:89]
	s_waitcnt lgkmcnt(3)
	v_mfma_f32_16x16x32_bf16 v[82:85], v[150:153], v[178:181], v[82:85]
	v_mfma_f32_16x16x32_bf16 v[74:77], v[154:157], v[178:181], v[74:77]
	v_mfma_f32_16x16x32_bf16 v[78:81], v[158:161], v[178:181], v[78:81]
	v_mfma_f32_16x16x32_bf16 v[70:73], v[162:165], v[178:181], v[70:73]
	s_waitcnt lgkmcnt(2)
	v_mfma_f32_16x16x32_bf16 v[66:69], v[150:153], v[174:177], v[66:69]
	v_mfma_f32_16x16x32_bf16 v[58:61], v[154:157], v[174:177], v[58:61]
	v_mfma_f32_16x16x32_bf16 v[62:65], v[158:161], v[174:177], v[62:65]
	v_mfma_f32_16x16x32_bf16 v[54:57], v[162:165], v[174:177], v[54:57]
	s_waitcnt lgkmcnt(1)
	v_mfma_f32_16x16x32_bf16 v[50:53], v[150:153], v[170:173], v[50:53]
	v_mfma_f32_16x16x32_bf16 v[42:45], v[154:157], v[170:173], v[42:45]
	v_mfma_f32_16x16x32_bf16 v[46:49], v[158:161], v[170:173], v[46:49]
	v_mfma_f32_16x16x32_bf16 v[38:41], v[162:165], v[170:173], v[38:41]
	s_waitcnt lgkmcnt(0)
	v_mfma_f32_16x16x32_bf16 v[34:37], v[150:153], v[166:169], v[34:37]
	v_mfma_f32_16x16x32_bf16 v[26:29], v[154:157], v[166:169], v[26:29]
	v_mfma_f32_16x16x32_bf16 v[30:33], v[158:161], v[166:169], v[30:33]
	v_mfma_f32_16x16x32_bf16 v[22:25], v[162:165], v[166:169], v[22:25]
